# final MoE-combine row phase: the 8 tok_info quads of a wave fetched once per block (one per lane) and picked with v_readlane, removing one exposed load round trip per row
# speedup vs baseline: 1.0087x; 1.0028x over previous
; #define LAS __attribute__((address_space(3)))
; template <int YMODE, int EXTRA, bool NORM_OUT, bool XN8  , bool XIN_BF = false  , bool XOUT_BF = false  > ...
;     ...
;         { const int col = 4 * F.tid;
;             if (YMODE) { const f32x4 g = *(const f32x4*)(gt + (size_t)b * 6 * D + col), p = *(const f32x4*)(gpost + col); *(LAS f32x4*)(vA + col) = g * p; }
;             if (NORM_OUT) { const f32x4 g = *(const f32x4*)(gpre + col), s = *(const f32x4*)(sc + (size_t)b * 6 * D + col); *(LAS f32x4*)(vB + col) = g * (1.f + s); *(LAS f32x4*)(vC + col) = *(const f32x4*)(sh + (size_t)b * 6 * D + col); } }
;         __syncthreads();
;         f32x4 xr[8]; u32x2 xrb[8], yr[8], yr2[8]; float w1n = 0.f, w2n = 0.f;
.LBB0_2454:
	s_ashr_i32 s3, s2, 31
	s_lshr_b32 s0, s3, 27
	s_add_i32 s0, s2, s0
	s_ashr_i32 s0, s0, 5
	s_mul_i32 s0, s0, 6
	s_ashr_i32 s1, s0, 31
	s_lshl_b64 s[0:1], s[0:1], 13
	s_waitcnt lgkmcnt(0)
	s_barrier
	v_lshl_add_u64 v[4:5], v[8:9], 0, s[0:1]
	global_load_dwordx4 v[0:3], v[10:11], off
	global_load_dwordx4 v[16:19], v[4:5], off
	s_lshl_b64 s[8:9], s[2:3], 6
	s_add_u32 s3, s8, s12
	s_addc_u32 s11, s9, 0
	s_and_b32 s0, s2, 7
	s_or_b32 s10, s3, s0
	s_lshl_b64 s[0:1], s[10:11], 12
	s_lshl_b64 s[16:17], s[10:11], 4
	s_add_u32 s16, s28, s16
	s_addc_u32 s17, s29, s17
	s_waitcnt vmcnt(0) lgkmcnt(0)
	v_pk_mul_f32 v[2:3], v[18:19], v[2:3]
	v_pk_mul_f32 v[0:1], v[16:17], v[0:1]
	ds_write_b128 v13, v[0:3]
	s_waitcnt lgkmcnt(0)
	s_barrier
	s_and_b32 s24, s10, 7
	s_andn2_b32 s22, s10, 7
	s_mov_b32 s23, s11
	s_lshl_b64 s[22:23], s[22:23], 4
	s_add_u32 s22, s28, s22
	s_addc_u32 s23, s29, s23
	v_and_b32_e32 v204, 7, v194
	v_lshlrev_b32_e32 v204, 4, v204
	global_load_dwordx4 v[196:199], v204, s[22:23]
	v_lshl_add_u64 v[0:1], v[14:15], 0, s[0:1]
	global_load_dwordx2 v[96:97], v[0:1], off nt
	global_load_dwordx2 v[94:95], v[0:1], off offset:512 nt
	global_load_dwordx2 v[92:93], v[0:1], off offset:1024 nt
	global_load_dwordx2 v[90:91], v[0:1], off offset:1536 nt
	global_load_dwordx2 v[86:87], v[0:1], off offset:2048 nt
	global_load_dwordx2 v[84:85], v[0:1], off offset:2560 nt
	global_load_dwordx2 v[82:83], v[0:1], off offset:3072 nt
	global_load_dwordx2 v[16:17], v[0:1], off offset:3584 nt
	s_waitcnt vmcnt(8)
	v_readlane_b32 s1, v196, s24
	v_readlane_b32 s0, v197, s24
	v_readlane_b32 s25, v198, s24
	v_readlane_b32 s26, v199, s24
	s_nop 1
	v_mov_b32_e32 v4, s25
	v_mov_b32_e32 v5, s26
	s_bfe_u32 s6, s1, 0x100010
	s_bfe_u32 s10, s0, 0x100010
	s_lshl_b32 s6, s6, 2
	s_lshl_b32 s10, s10, 2
	s_add_i32 s6, s13, s6
	s_add_i32 s10, s13, s10
	v_mov_b32_e32 v0, s6
	v_mov_b32_e32 v1, s10
	ds_read_b32 v0, v0
	ds_read_b32 v2, v1
	s_lshl_b32 s1, s1, 12
	s_lshl_b32 s0, s0, 12
	s_and_b32 s6, s1, 0xffff000
	s_waitcnt lgkmcnt(1)
	v_ashrrev_i32_e32 v1, 31, v0
	s_waitcnt lgkmcnt(0)
	v_ashrrev_i32_e32 v3, 31, v2
	v_lshlrev_b64 v[0:1], 20, v[0:1]
	v_lshlrev_b64 v[2:3], 20, v[2:3]
	v_lshl_add_u64 v[0:1], s[72:73], 0, v[0:1]
	v_lshl_add_u64 v[2:3], s[72:73], 0, v[2:3]
	v_lshl_add_u64 v[0:1], v[0:1], 0, s[6:7]
	s_and_b32 s6, s0, 0xffff000
	v_lshl_add_u64 v[2:3], v[2:3], 0, s[6:7]
	v_readfirstlane_b32 s0, v0
	v_readfirstlane_b32 s1, v1
	v_readfirstlane_b32 s16, v2
	v_readfirstlane_b32 s17, v3
	s_nop 2
	global_load_dwordx2 v[108:109], v126, s[0:1] nt
	global_load_dwordx2 v[106:107], v126, s[0:1] offset:512 nt
	global_load_dwordx2 v[102:103], v126, s[0:1] offset:1024 nt
	global_load_dwordx2 v[98:99], v126, s[0:1] offset:1536 nt
	global_load_dwordx2 v[104:105], v126, s[16:17] nt
	global_load_dwordx2 v[100:101], v126, s[16:17] offset:512 nt
	global_load_dwordx2 v[80:81], v126, s[16:17] offset:1024 nt
	global_load_dwordx2 v[76:77], v126, s[16:17] offset:1536 nt
	global_load_dwordx2 v[72:73], v126, s[16:17] offset:2048 nt
	global_load_dwordx2 v[68:69], v126, s[16:17] offset:2560 nt
	global_load_dwordx2 v[66:67], v126, s[16:17] offset:3072 nt
	global_load_dwordx2 v[64:65], v126, s[16:17] offset:3584 nt
	global_load_dwordx2 v[88:89], v126, s[0:1] offset:2048 nt
	global_load_dwordx2 v[78:79], v126, s[0:1] offset:2560 nt
	global_load_dwordx2 v[74:75], v126, s[0:1] offset:3072 nt
	global_load_dwordx2 v[70:71], v126, s[0:1] offset:3584 nt
	s_mov_b32 s16, s7
	s_waitcnt vmcnt(11)
	v_mov_b64_e32 v[0:1], v[104:105]
	s_waitcnt vmcnt(10)
	v_mov_b64_e32 v[18:19], v[100:101]
	s_waitcnt vmcnt(9)
	v_mov_b64_e32 v[20:21], v[80:81]
	s_waitcnt vmcnt(8)
	v_mov_b64_e32 v[22:23], v[76:77]
	s_waitcnt vmcnt(7)
	v_mov_b64_e32 v[24:25], v[72:73]
	s_waitcnt vmcnt(6)
	v_mov_b64_e32 v[26:27], v[68:69]
	s_waitcnt vmcnt(5)
	v_mov_b64_e32 v[28:29], v[66:67]
	s_waitcnt vmcnt(4)
	v_mov_b64_e32 v[30:31], v[64:65]
	s_branch .LBB0_2456

; template <int YMODE, int EXTRA, bool NORM_OUT, bool XN8  , bool XIN_BF = false  , bool XOUT_BF = false  > ...
;     ...
;             if (rr < 7) RP_LOAD(rr + 1);
.LBB0_2456:
	s_add_i32 s0, s2, s16
	s_cmp_eq_u32 s16, 7
	v_mov_b64_e32 v[2:3], v[4:5]
	v_mov_b32_e32 v48, v108
	v_mov_b32_e32 v49, v109
	v_mov_b32_e32 v50, v106
	v_mov_b32_e32 v51, v107
	v_mov_b32_e32 v52, v102
	v_mov_b32_e32 v53, v103
	v_mov_b32_e32 v54, v98
	v_mov_b32_e32 v55, v99
	s_waitcnt vmcnt(3)
	v_mov_b32_e32 v56, v88
	v_mov_b32_e32 v57, v89
	s_waitcnt vmcnt(2)
	v_mov_b32_e32 v58, v78
	v_mov_b32_e32 v59, v79
	s_waitcnt vmcnt(1)
	v_mov_b32_e32 v60, v74
	v_mov_b32_e32 v61, v75
	s_waitcnt vmcnt(0)
	v_mov_b32_e32 v62, v70
	v_mov_b32_e32 v63, v71
	v_mov_b32_e32 v32, v96
	v_mov_b32_e32 v33, v97
	v_mov_b32_e32 v34, v94
	v_mov_b32_e32 v35, v95
	v_mov_b32_e32 v36, v92
	v_mov_b32_e32 v37, v93
	v_mov_b32_e32 v38, v90
	v_mov_b32_e32 v39, v91
	v_mov_b32_e32 v40, v86
	v_mov_b32_e32 v41, v87
	v_mov_b32_e32 v42, v84
	v_mov_b32_e32 v43, v85
	v_mov_b32_e32 v44, v82
	v_mov_b32_e32 v45, v83
	v_mov_b32_e32 v46, v16
	v_mov_b32_e32 v47, v17
	s_cbranch_scc1 .LBB0_2455
	s_add_i32 s1, s0, 1
	s_and_b32 s1, s1, 7
	s_mov_b32 s24, s1
	s_or_b32 s10, s3, s1
	s_lshl_b64 s[18:19], s[10:11], 12
	s_lshl_b64 s[20:21], s[10:11], 4
	s_add_u32 s20, s28, s20
	s_addc_u32 s21, s29, s21
	global_load_dwordx4 v[200:203], v7, s[20:21]
	v_lshl_add_u64 v[18:19], v[14:15], 0, s[18:19]
	global_load_dwordx2 v[32:33], v[18:19], off nt
	global_load_dwordx2 v[34:35], v[18:19], off offset:512 nt
	global_load_dwordx2 v[36:37], v[18:19], off offset:1024 nt
	global_load_dwordx2 v[38:39], v[18:19], off offset:1536 nt
	global_load_dwordx2 v[40:41], v[18:19], off offset:2048 nt
	global_load_dwordx2 v[42:43], v[18:19], off offset:2560 nt
	global_load_dwordx2 v[44:45], v[18:19], off offset:3072 nt
	global_load_dwordx2 v[46:47], v[18:19], off offset:3584 nt
	v_readlane_b32 s6, v196, s24
	v_readlane_b32 s1, v197, s24
	v_readlane_b32 s25, v198, s24
	v_readlane_b32 s26, v199, s24
	s_nop 1
	v_mov_b32_e32 v2, s25
	v_mov_b32_e32 v3, s26
	s_bfe_u32 s10, s6, 0x100010
	s_bfe_u32 s17, s1, 0x100010
	s_lshl_b32 s10, s10, 2
	s_lshl_b32 s17, s17, 2
	s_add_i32 s10, s13, s10
	s_add_i32 s17, s13, s17
	v_mov_b32_e32 v0, s10
	v_mov_b32_e32 v1, s17
	ds_read_b32 v0, v0
	ds_read_b32 v18, v1
	s_lshl_b32 s6, s6, 12
	s_lshl_b32 s1, s1, 12
	s_and_b32 s6, s6, 0xffff000
	s_waitcnt lgkmcnt(1)
	v_ashrrev_i32_e32 v1, 31, v0
	s_waitcnt lgkmcnt(0)
	v_ashrrev_i32_e32 v19, 31, v18
	v_lshlrev_b64 v[0:1], 20, v[0:1]
	v_lshlrev_b64 v[18:19], 20, v[18:19]
	v_lshl_add_u64 v[0:1], s[72:73], 0, v[0:1]
	v_lshl_add_u64 v[18:19], s[72:73], 0, v[18:19]
	v_lshl_add_u64 v[0:1], v[0:1], 0, s[6:7]
	s_and_b32 s6, s1, 0xffff000
	v_lshl_add_u64 v[18:19], v[18:19], 0, s[6:7]
	v_readfirstlane_b32 s18, v0
	v_readfirstlane_b32 s19, v1
	v_readfirstlane_b32 s20, v18
	v_readfirstlane_b32 s21, v19
	s_nop 2
	global_load_dwordx2 v[48:49], v126, s[18:19] nt
	global_load_dwordx2 v[50:51], v126, s[18:19] offset:512 nt
	global_load_dwordx2 v[52:53], v126, s[18:19] offset:1024 nt
	global_load_dwordx2 v[54:55], v126, s[18:19] offset:1536 nt
	global_load_dwordx2 v[56:57], v126, s[18:19] offset:2048 nt
	global_load_dwordx2 v[58:59], v126, s[18:19] offset:2560 nt
	global_load_dwordx2 v[60:61], v126, s[18:19] offset:3072 nt
	global_load_dwordx2 v[62:63], v126, s[18:19] offset:3584 nt
	global_load_dwordx2 v[0:1], v126, s[20:21] nt
	global_load_dwordx2 v[18:19], v126, s[20:21] offset:512 nt
	global_load_dwordx2 v[20:21], v126, s[20:21] offset:1024 nt
	global_load_dwordx2 v[22:23], v126, s[20:21] offset:1536 nt
	global_load_dwordx2 v[24:25], v126, s[20:21] offset:2048 nt
	global_load_dwordx2 v[26:27], v126, s[20:21] offset:2560 nt
	global_load_dwordx2 v[28:29], v126, s[20:21] offset:3072 nt
	global_load_dwordx2 v[30:31], v126, s[20:21] offset:3584 nt
	s_branch .LBB0_2455
